# speedup vs baseline: 1.0041x; 1.0041x over previous
.LBB3_2:
	s_load_dword s0, s[0:1], 0x20
	s_and_b32 s14, s2, 7
	v_cvt_f32_ubyte0_e32 v3, s14
	v_lshlrev_b32_e32 v100, 4, v0
	s_mov_b64 s[18:19], 0x20080
	s_waitcnt lgkmcnt(0)
	s_ashr_i32 s1, s0, 31
	s_lshr_b32 s1, s1, 22
	s_add_i32 s1, s0, s1
	s_ashr_i32 s3, s1, 10
	v_cvt_f32_i32_e32 v1, s3
	s_ashr_i32 s1, s1, 31
	s_or_b32 s1, s1, 1
	s_movk_i32 s17, 0x70
	v_rcp_iflag_f32_e32 v2, v1
	s_nop 0
	v_mul_f32_e32 v2, v3, v2
	v_trunc_f32_e32 v2, v2
	v_fma_f32 v3, -v2, v1, v3
	v_cvt_i32_f32_e32 v2, v2
	v_cmp_ge_f32_e64 s[12:13], |v3|, |v1|
	s_and_b64 s[12:13], s[12:13], exec
	s_cselect_b32 s1, s1, 0
	v_readfirstlane_b32 s13, v2
	s_add_i32 s1, s13, s1
	s_lshl_b32 s12, s2, 4
	s_bfe_i32 s13, s1, 0x160000
	s_mul_i32 s1, s1, s3
	s_and_b32 s12, s12, 0x180
	s_sub_i32 s3, s14, s1
	s_lshl_b32 s1, s13, 9
	s_or_b32 s1, s1, s12
	s_lshl_b32 s2, s2, 2
	v_lshrrev_b32_e32 v1, 3, v0
	v_lshrrev_b32_e32 v2, 4, v0
	s_lshl_b32 s3, s3, 10
	s_and_b32 s2, s2, 0xffffff80
	v_xor_b32_e32 v10, v2, v0
	v_or_b32_e32 v2, s1, v1
	s_add_i32 s2, s3, s2
	v_and_b32_e32 v104, 15, v0
	v_lshlrev_b32_e32 v104, 2, v104
	v_and_b32_e32 v105, 64, v0
	v_or3_b32 v104, v104, v105, s2
	v_mov_b32_e32 v105, 0
	v_lshlrev_b64 v[104:105], 2, v[104:105]
	v_lshl_add_u64 v[104:105], s[10:11], 0, v[104:105]
	global_load_dwordx4 v[106:109], v[104:105], off
	v_ashrrev_i32_e32 v3, 31, v2
	v_lshlrev_b64 v[4:5], 11, v[2:3]
	v_or_b32_e32 v2, s2, v1
	v_mov_b32_e32 v3, 0
	v_lshlrev_b32_e32 v1, 4, v10
	v_lshlrev_b64 v[6:7], 11, v[2:3]
	v_and_b32_e32 v2, 0x70, v1
	v_add_u32_e32 v1, 0, v100
	v_lshl_add_u64 v[8:9], s[6:7], 0, v[6:7]
	v_lshl_add_u64 v[4:5], s[4:5], 0, v[4:5]
	v_readfirstlane_b32 s6, v1
	v_add_u32_e32 v10, 0x2000, v1
	v_lshl_add_u64 v[6:7], v[4:5], 0, v[2:3]
	v_lshl_add_u64 v[4:5], v[8:9], 0, v[2:3]
	v_add_u32_e32 v2, 0x4000, v1
	s_mov_b32 m0, s6
	s_mov_b64 s[12:13], 0x20000
	v_readfirstlane_b32 s3, v10
	global_load_lds_dwordx4 v[6:7], off
	v_lshl_add_u64 v[8:9], v[6:7], 0, s[12:13]
	s_mov_b32 m0, s3
	v_readfirstlane_b32 s4, v2
	v_add_u32_e32 v2, 0x6000, v1
	global_load_lds_dwordx4 v[8:9], off
	s_mov_b32 m0, s4
	v_readfirstlane_b32 s5, v2
	v_add_u32_e32 v12, 0x8000, v1
	global_load_lds_dwordx4 v[4:5], off
	v_lshl_add_u64 v[8:9], v[4:5], 0, s[12:13]
	s_mov_b32 m0, s5
	s_mov_b64 s[12:13], 0x80
	v_readfirstlane_b32 s16, v12
	v_add_u32_e32 v12, 0xa000, v1
	global_load_lds_dwordx4 v[8:9], off
	v_lshl_add_u64 v[8:9], v[4:5], 0, s[12:13]
	v_add_u32_e32 v2, 0xc000, v1
	v_lshl_add_u64 v[10:11], v[6:7], 0, s[12:13]
	s_mov_b32 m0, s16
	v_readfirstlane_b32 s13, v12
	global_load_lds_dwordx4 v[10:11], off
	v_lshl_add_u64 v[10:11], v[6:7], 0, s[18:19]
	s_mov_b32 m0, s13
	v_readfirstlane_b32 s14, v2
	v_add_u32_e32 v2, 0xe000, v1
	global_load_lds_dwordx4 v[10:11], off
	s_mov_b32 m0, s14
	v_readfirstlane_b32 s15, v2
	s_add_i32 s7, 0, 0x14000
	v_add_u32_e32 v12, 0x10000, v1
	global_load_lds_dwordx4 v[8:9], off
	v_lshl_add_u64 v[8:9], v[4:5], 0, s[18:19]
	s_mov_b32 m0, s15
	s_mov_b64 s[18:19], 0x100
	v_add_u32_e32 v2, s7, v100
	v_readfirstlane_b32 s7, v12
	v_add_u32_e32 v1, 0x12000, v1
	global_load_lds_dwordx4 v[8:9], off
	v_lshl_add_u64 v[8:9], v[4:5], 0, s[18:19]
	v_lshl_add_u64 v[10:11], v[6:7], 0, s[18:19]
	s_mov_b32 m0, s7
	s_mov_b64 s[18:19], 0x20100
	v_readfirstlane_b32 s7, v1
	global_load_lds_dwordx4 v[10:11], off
	v_lshl_add_u64 v[10:11], v[6:7], 0, s[18:19]
	s_mov_b32 m0, s7
	v_readfirstlane_b32 s7, v2
	v_add_u32_e32 v1, 0x2000, v2
	global_load_lds_dwordx4 v[10:11], off
	s_mov_b32 m0, s7
	v_readfirstlane_b32 s12, v1
	global_load_lds_dwordx4 v[8:9], off
	v_lshl_add_u64 v[8:9], v[4:5], 0, s[18:19]
	s_mov_b32 m0, s12
	v_lshrrev_b32_e32 v1, 2, v0
	global_load_lds_dwordx4 v[8:9], off
	v_and_b32_e32 v8, 15, v0
	v_and_b32_e32 v1, 0x60, v1
	v_or_b32_e32 v10, v1, v8
	v_lshlrev_b32_e32 v101, 7, v10
	v_lshlrev_b32_e32 v10, 7, v0
	v_and_b32_e32 v2, 63, v0
	v_lshlrev_b32_e32 v9, 3, v0
	v_and_b32_e32 v102, 0x2780, v10
	v_bitop3_b32 v10, v2, s17, v9 bitop3:0x48
	v_add_u32_e32 v56, 0, v102
	v_add_u32_e32 v48, 0, v101
	s_waitcnt vmcnt(8) lgkmcnt(0)
	s_barrier
	v_add_u32_e32 v2, v56, v10
	v_add_u32_e32 v11, v48, v10
	v_bitop3_b32 v9, v0, v9, 63 bitop3:0x6c
	v_mov_b32_e32 v10, 0x70
	ds_read_b128 v[12:15], v2 offset:16384
	ds_read_b128 v[16:19], v2 offset:18432
	ds_read_b128 v[20:23], v11
	ds_read_b128 v[24:27], v11 offset:2048
	ds_read_b128 v[32:35], v2 offset:20480
	ds_read_b128 v[40:43], v2 offset:22528
	v_bitop3_b32 v103, v9, 64, v10 bitop3:0x6c
	v_add_u32_e32 v10, v48, v103
	v_add_u32_e32 v9, v56, v103
	ds_read_b128 v[48:51], v10
	ds_read_b128 v[52:55], v10 offset:2048
	ds_read_b128 v[56:59], v9 offset:16384
	ds_read_b128 v[60:63], v9 offset:18432
	ds_read_b128 v[64:67], v9 offset:20480
	ds_read_b128 v[68:71], v9 offset:22528
	s_waitcnt lgkmcnt(0)
	v_mfma_f32_16x16x32_f16 v[28:31], v[12:15], v[20:23], 0
	v_mfma_f32_16x16x32_f16 v[36:39], v[16:19], v[20:23], 0
	v_mfma_f32_16x16x32_f16 v[44:47], v[32:35], v[20:23], 0
	v_mfma_f32_16x16x32_f16 v[20:23], v[40:43], v[20:23], 0
	v_mfma_f32_16x16x32_f16 v[12:15], v[12:15], v[24:27], 0
	v_mfma_f32_16x16x32_f16 v[16:19], v[16:19], v[24:27], 0
	v_mfma_f32_16x16x32_f16 v[32:35], v[32:35], v[24:27], 0
	v_mfma_f32_16x16x32_f16 v[24:27], v[40:43], v[24:27], 0
	s_mov_b64 s[18:19], 0x180
	s_mov_b32 m0, s6
	s_waitcnt vmcnt(4) lgkmcnt(0)
	s_barrier
	v_lshl_add_u64 v[40:41], v[4:5], 0, s[18:19]
	v_lshl_add_u64 v[42:43], v[6:7], 0, s[18:19]
	s_mov_b64 s[18:19], 0x20180
	global_load_lds_dwordx4 v[42:43], off
	v_lshl_add_u64 v[42:43], v[6:7], 0, s[18:19]
	s_mov_b32 m0, s3
	s_nop 0
	global_load_lds_dwordx4 v[42:43], off
	s_mov_b32 m0, s4
	s_nop 0
	global_load_lds_dwordx4 v[40:41], off
	v_lshl_add_u64 v[40:41], v[4:5], 0, s[18:19]
	s_mov_b32 m0, s5
	s_nop 0
	global_load_lds_dwordx4 v[40:41], off
	ds_read_b128 v[40:43], v11 offset:32768
	ds_read_b128 v[72:75], v11 offset:34816
	ds_read_b128 v[76:79], v2 offset:49152
	ds_read_b128 v[80:83], v2 offset:51200
	ds_read_b128 v[84:87], v2 offset:53248
	ds_read_b128 v[88:91], v2 offset:55296
	v_mfma_f32_16x16x32_f16 v[28:31], v[56:59], v[48:51], v[28:31]
	v_mfma_f32_16x16x32_f16 v[36:39], v[60:63], v[48:51], v[36:39]
	v_mfma_f32_16x16x32_f16 v[44:47], v[64:67], v[48:51], v[44:47]
	v_mfma_f32_16x16x32_f16 v[20:23], v[68:71], v[48:51], v[20:23]
	v_mfma_f32_16x16x32_f16 v[12:15], v[56:59], v[52:55], v[12:15]
	v_mfma_f32_16x16x32_f16 v[16:19], v[60:63], v[52:55], v[16:19]
	v_mfma_f32_16x16x32_f16 v[32:35], v[64:67], v[52:55], v[32:35]
	v_mfma_f32_16x16x32_f16 v[24:27], v[68:71], v[52:55], v[24:27]
	s_waitcnt lgkmcnt(0)
	v_mfma_f32_16x16x32_f16 v[28:31], v[76:79], v[40:43], v[28:31]
	ds_read_b128 v[52:55], v10 offset:32768
	ds_read_b128 v[56:59], v10 offset:34816
	v_mfma_f32_16x16x32_f16 v[36:39], v[80:83], v[40:43], v[36:39]
	v_mfma_f32_16x16x32_f16 v[44:47], v[84:87], v[40:43], v[44:47]
	v_mfma_f32_16x16x32_f16 v[20:23], v[88:91], v[40:43], v[20:23]
	v_mfma_f32_16x16x32_f16 v[40:43], v[76:79], v[72:75], v[12:15]
	ds_read_b128 v[60:63], v9 offset:49152
	ds_read_b128 v[64:67], v9 offset:51200
	ds_read_b128 v[68:71], v9 offset:53248
	ds_read_b128 v[76:79], v9 offset:55296
	v_mfma_f32_16x16x32_f16 v[48:51], v[80:83], v[72:75], v[16:19]
	v_mfma_f32_16x16x32_f16 v[32:35], v[84:87], v[72:75], v[32:35]
	v_mfma_f32_16x16x32_f16 v[24:27], v[88:91], v[72:75], v[24:27]
	s_mov_b64 s[18:19], 0x200
	s_mov_b32 m0, s16
	s_waitcnt vmcnt(4) lgkmcnt(0)
	s_barrier
	v_lshl_add_u64 v[12:13], v[4:5], 0, s[18:19]
	v_lshl_add_u64 v[14:15], v[6:7], 0, s[18:19]
	s_mov_b64 s[18:19], 0x20200
	global_load_lds_dwordx4 v[14:15], off
	v_lshl_add_u64 v[14:15], v[6:7], 0, s[18:19]
	s_mov_b32 m0, s13
	v_add_u32_e32 v16, 0x15000, v2
	global_load_lds_dwordx4 v[14:15], off
	s_mov_b32 m0, s14
	v_add_u32_e32 v14, 0x14000, v2
	global_load_lds_dwordx4 v[12:13], off
	v_lshl_add_u64 v[12:13], v[4:5], 0, s[18:19]
	s_mov_b32 m0, s15
	v_add_u32_e32 v15, 0x14800, v2
	global_load_lds_dwordx4 v[12:13], off
	v_add_u32_e32 v12, 0x10000, v11
	v_add_u32_e32 v13, 0x10800, v11
	ds_read_b128 v[72:75], v12
	ds_read_b128 v[80:83], v13
	ds_read_b128 v[84:87], v14
	ds_read_b128 v[88:91], v15
	v_add_u32_e32 v17, 0x15800, v2
	ds_read_b128 v[92:95], v16
	ds_read_b128 v[96:99], v17
	v_mfma_f32_16x16x32_f16 v[28:31], v[60:63], v[52:55], v[28:31]
	v_mfma_f32_16x16x32_f16 v[36:39], v[64:67], v[52:55], v[36:39]
	v_mfma_f32_16x16x32_f16 v[44:47], v[68:71], v[52:55], v[44:47]
	v_mfma_f32_16x16x32_f16 v[18:21], v[76:79], v[52:55], v[20:23]
	v_mfma_f32_16x16x32_f16 v[40:43], v[60:63], v[56:59], v[40:43]
	v_mfma_f32_16x16x32_f16 v[48:51], v[64:67], v[56:59], v[48:51]
	v_mfma_f32_16x16x32_f16 v[32:35], v[68:71], v[56:59], v[32:35]
	v_mfma_f32_16x16x32_f16 v[22:25], v[76:79], v[56:59], v[24:27]
	s_add_i32 s17, 0, 0x10000
	s_waitcnt lgkmcnt(0)
	v_mfma_f32_16x16x32_f16 v[52:55], v[96:99], v[72:75], v[18:21]
	s_nop 2
	v_add_u32_e32 v18, s17, v103
	v_add_u32_e32 v19, v18, v101
	v_add_u32_e32 v18, v18, v102
	v_mfma_f32_16x16x32_f16 v[26:29], v[84:87], v[72:75], v[28:31]
	ds_read_b128 v[56:59], v19
	ds_read_b128 v[60:63], v19 offset:2048
	v_mfma_f32_16x16x32_f16 v[36:39], v[88:91], v[72:75], v[36:39]
	v_mfma_f32_16x16x32_f16 v[44:47], v[92:95], v[72:75], v[44:47]
	ds_read_b128 v[64:67], v18 offset:16384
	ds_read_b128 v[68:71], v18 offset:18432
	ds_read_b128 v[72:75], v18 offset:20480
	ds_read_b128 v[76:79], v18 offset:22528
	v_mfma_f32_16x16x32_f16 v[40:43], v[84:87], v[80:83], v[40:43]
	v_mfma_f32_16x16x32_f16 v[48:51], v[88:91], v[80:83], v[48:51]
	v_mfma_f32_16x16x32_f16 v[30:33], v[92:95], v[80:83], v[32:35]
	v_mfma_f32_16x16x32_f16 v[20:23], v[96:99], v[80:83], v[22:25]
	s_mov_b64 s[18:19], 0x280
	v_add_u32_e32 v80, s17, v100
	s_nop 0
	v_lshl_add_u64 v[24:25], v[4:5], 0, s[18:19]
	v_lshl_add_u64 v[34:35], v[6:7], 0, s[18:19]
	v_readfirstlane_b32 s18, v80
	v_add_u32_e32 v80, 0x2000, v80
	s_waitcnt vmcnt(4) lgkmcnt(0)
	s_barrier
	s_mov_b32 m0, s18
	s_mov_b64 s[20:21], 0x20280
	v_readfirstlane_b32 s17, v80
	global_load_lds_dwordx4 v[34:35], off
	v_lshl_add_u64 v[34:35], v[6:7], 0, s[20:21]
	s_mov_b32 m0, s17
	s_nop 0
	global_load_lds_dwordx4 v[34:35], off
	s_mov_b32 m0, s7
	s_nop 0
	global_load_lds_dwordx4 v[24:25], off
	v_lshl_add_u64 v[24:25], v[4:5], 0, s[20:21]
	s_mov_b32 m0, s12
	s_nop 0
	global_load_lds_dwordx4 v[24:25], off
	ds_read_b128 v[80:83], v11
	ds_read_b128 v[84:87], v11 offset:2048
	ds_read_b128 v[88:91], v2 offset:16384
	ds_read_b128 v[92:95], v2 offset:18432
	ds_read_b128 v[96:99], v2 offset:20480
	ds_read_b128 v[100:103], v2 offset:22528
	v_mfma_f32_16x16x32_f16 v[24:27], v[64:67], v[56:59], v[26:29]
	v_mfma_f32_16x16x32_f16 v[34:37], v[68:71], v[56:59], v[36:39]
	v_mfma_f32_16x16x32_f16 v[44:47], v[72:75], v[56:59], v[44:47]
	v_mfma_f32_16x16x32_f16 v[52:55], v[76:79], v[56:59], v[52:55]
	v_mfma_f32_16x16x32_f16 v[38:41], v[64:67], v[60:63], v[40:43]
	v_mfma_f32_16x16x32_f16 v[48:51], v[68:71], v[60:63], v[48:51]
	v_mfma_f32_16x16x32_f16 v[28:31], v[72:75], v[60:63], v[30:33]
	v_mfma_f32_16x16x32_f16 v[20:23], v[76:79], v[60:63], v[20:23]
	ds_read_b128 v[56:59], v10
	ds_read_b128 v[60:63], v10 offset:2048
	ds_read_b128 v[64:67], v9 offset:16384
	ds_read_b128 v[68:71], v9 offset:18432
	ds_read_b128 v[72:75], v9 offset:20480
	ds_read_b128 v[76:79], v9 offset:22528
	s_waitcnt lgkmcnt(0)
	v_mfma_f32_16x16x32_f16 v[24:27], v[88:91], v[80:83], v[24:27]
	v_mfma_f32_16x16x32_f16 v[32:35], v[92:95], v[80:83], v[34:37]
	v_mfma_f32_16x16x32_f16 v[42:45], v[96:99], v[80:83], v[44:47]
	v_mfma_f32_16x16x32_f16 v[52:55], v[100:103], v[80:83], v[52:55]
	v_mfma_f32_16x16x32_f16 v[36:39], v[88:91], v[84:87], v[38:41]
	v_mfma_f32_16x16x32_f16 v[46:49], v[92:95], v[84:87], v[48:51]
	v_mfma_f32_16x16x32_f16 v[28:31], v[96:99], v[84:87], v[28:31]
	v_mfma_f32_16x16x32_f16 v[20:23], v[100:103], v[84:87], v[20:23]
	s_mov_b64 s[20:21], 0x300
	s_mov_b32 m0, s6
	s_waitcnt vmcnt(4) lgkmcnt(0)
	s_barrier
	v_lshl_add_u64 v[40:41], v[4:5], 0, s[20:21]
	v_lshl_add_u64 v[50:51], v[6:7], 0, s[20:21]
	s_mov_b64 s[20:21], 0x20300
	global_load_lds_dwordx4 v[50:51], off
	v_lshl_add_u64 v[50:51], v[6:7], 0, s[20:21]
	s_mov_b32 m0, s3
	s_nop 0
	global_load_lds_dwordx4 v[50:51], off
	s_mov_b32 m0, s4
	s_nop 0
	global_load_lds_dwordx4 v[40:41], off
	v_lshl_add_u64 v[40:41], v[4:5], 0, s[20:21]
	s_mov_b32 m0, s5
	s_nop 0
	global_load_lds_dwordx4 v[40:41], off
	ds_read_b128 v[80:83], v11 offset:32768
	ds_read_b128 v[84:87], v11 offset:34816
	ds_read_b128 v[88:91], v2 offset:49152
	ds_read_b128 v[92:95], v2 offset:51200
	ds_read_b128 v[96:99], v2 offset:53248
	ds_read_b128 v[100:103], v2 offset:55296
	v_mfma_f32_16x16x32_f16 v[24:27], v[64:67], v[56:59], v[24:27]
	v_mfma_f32_16x16x32_f16 v[32:35], v[68:71], v[56:59], v[32:35]
	v_mfma_f32_16x16x32_f16 v[40:43], v[72:75], v[56:59], v[42:45]
	v_mfma_f32_16x16x32_f16 v[50:53], v[76:79], v[56:59], v[52:55]
	v_mfma_f32_16x16x32_f16 v[36:39], v[64:67], v[60:63], v[36:39]
	v_mfma_f32_16x16x32_f16 v[44:47], v[68:71], v[60:63], v[46:49]
	v_mfma_f32_16x16x32_f16 v[28:31], v[72:75], v[60:63], v[28:31]
	v_mfma_f32_16x16x32_f16 v[20:23], v[76:79], v[60:63], v[20:23]
	s_waitcnt lgkmcnt(0)
	v_mfma_f32_16x16x32_f16 v[48:51], v[100:103], v[80:83], v[50:53]
	s_nop 2
	ds_read_b128 v[52:55], v10 offset:32768
	ds_read_b128 v[56:59], v10 offset:34816
	ds_read_b128 v[60:63], v9 offset:49152
	ds_read_b128 v[64:67], v9 offset:51200
	ds_read_b128 v[68:71], v9 offset:53248
	ds_read_b128 v[72:75], v9 offset:55296
	v_mfma_f32_16x16x32_f16 v[24:27], v[88:91], v[80:83], v[24:27]
	v_mfma_f32_16x16x32_f16 v[32:35], v[92:95], v[80:83], v[32:35]
	v_mfma_f32_16x16x32_f16 v[40:43], v[96:99], v[80:83], v[40:43]
	v_mfma_f32_16x16x32_f16 v[36:39], v[88:91], v[84:87], v[36:39]
	v_mfma_f32_16x16x32_f16 v[44:47], v[92:95], v[84:87], v[44:47]
	v_mfma_f32_16x16x32_f16 v[28:31], v[96:99], v[84:87], v[28:31]
	v_mfma_f32_16x16x32_f16 v[20:23], v[100:103], v[84:87], v[20:23]
	s_mov_b64 s[20:21], 0x380
	s_mov_b32 m0, s16
	s_waitcnt vmcnt(4) lgkmcnt(0)
	s_barrier
	v_lshl_add_u64 v[76:77], v[4:5], 0, s[20:21]
	v_lshl_add_u64 v[78:79], v[6:7], 0, s[20:21]
	s_mov_b64 s[20:21], 0x20380
	global_load_lds_dwordx4 v[78:79], off
	v_lshl_add_u64 v[78:79], v[6:7], 0, s[20:21]
	s_mov_b32 m0, s13
	s_nop 0
	global_load_lds_dwordx4 v[78:79], off
	s_mov_b32 m0, s14
	s_nop 0
	global_load_lds_dwordx4 v[76:77], off
	v_lshl_add_u64 v[76:77], v[4:5], 0, s[20:21]
	s_mov_b32 m0, s15
	s_nop 0
	global_load_lds_dwordx4 v[76:77], off
	ds_read_b128 v[76:79], v12
	ds_read_b128 v[80:83], v13
	ds_read_b128 v[84:87], v14
	ds_read_b128 v[88:91], v15
	ds_read_b128 v[92:95], v16
	ds_read_b128 v[96:99], v17
	v_mfma_f32_16x16x32_f16 v[24:27], v[60:63], v[52:55], v[24:27]
	v_mfma_f32_16x16x32_f16 v[32:35], v[64:67], v[52:55], v[32:35]
	v_mfma_f32_16x16x32_f16 v[40:43], v[68:71], v[52:55], v[40:43]
	v_mfma_f32_16x16x32_f16 v[48:51], v[72:75], v[52:55], v[48:51]
	v_mfma_f32_16x16x32_f16 v[36:39], v[60:63], v[56:59], v[36:39]
	v_mfma_f32_16x16x32_f16 v[44:47], v[64:67], v[56:59], v[44:47]
	v_mfma_f32_16x16x32_f16 v[28:31], v[68:71], v[56:59], v[28:31]
	v_mfma_f32_16x16x32_f16 v[20:23], v[72:75], v[56:59], v[20:23]
	ds_read_b128 v[52:55], v19
	ds_read_b128 v[56:59], v19 offset:2048
	ds_read_b128 v[60:63], v18 offset:16384
	ds_read_b128 v[64:67], v18 offset:18432
	ds_read_b128 v[68:71], v18 offset:20480
	ds_read_b128 v[72:75], v18 offset:22528
	s_waitcnt lgkmcnt(0)
	v_mfma_f32_16x16x32_f16 v[24:27], v[84:87], v[76:79], v[24:27]
	v_mfma_f32_16x16x32_f16 v[32:35], v[88:91], v[76:79], v[32:35]
	v_mfma_f32_16x16x32_f16 v[40:43], v[92:95], v[76:79], v[40:43]
	v_mfma_f32_16x16x32_f16 v[48:51], v[96:99], v[76:79], v[48:51]
	v_mfma_f32_16x16x32_f16 v[36:39], v[84:87], v[80:83], v[36:39]
	v_mfma_f32_16x16x32_f16 v[44:47], v[88:91], v[80:83], v[44:47]
	v_mfma_f32_16x16x32_f16 v[28:31], v[92:95], v[80:83], v[28:31]
	v_mfma_f32_16x16x32_f16 v[20:23], v[96:99], v[80:83], v[20:23]
	s_mov_b64 s[20:21], 0x400
	s_mov_b32 m0, s18
	s_waitcnt vmcnt(4) lgkmcnt(0)
	s_barrier
	v_lshl_add_u64 v[76:77], v[4:5], 0, s[20:21]
	v_lshl_add_u64 v[78:79], v[6:7], 0, s[20:21]
	s_mov_b64 s[20:21], 0x20400
	global_load_lds_dwordx4 v[78:79], off
	v_lshl_add_u64 v[78:79], v[6:7], 0, s[20:21]
	s_mov_b32 m0, s17
	s_nop 0
	global_load_lds_dwordx4 v[78:79], off
	s_mov_b32 m0, s7
	s_nop 0
	global_load_lds_dwordx4 v[76:77], off
	v_lshl_add_u64 v[76:77], v[4:5], 0, s[20:21]
	s_mov_b32 m0, s12
	s_nop 0
	global_load_lds_dwordx4 v[76:77], off
	ds_read_b128 v[76:79], v11
	ds_read_b128 v[80:83], v11 offset:2048
	ds_read_b128 v[84:87], v2 offset:16384
	ds_read_b128 v[88:91], v2 offset:18432
	ds_read_b128 v[92:95], v2 offset:20480
	ds_read_b128 v[96:99], v2 offset:22528
	v_mfma_f32_16x16x32_f16 v[24:27], v[60:63], v[52:55], v[24:27]
	v_mfma_f32_16x16x32_f16 v[32:35], v[64:67], v[52:55], v[32:35]
	v_mfma_f32_16x16x32_f16 v[40:43], v[68:71], v[52:55], v[40:43]
	v_mfma_f32_16x16x32_f16 v[48:51], v[72:75], v[52:55], v[48:51]
	v_mfma_f32_16x16x32_f16 v[36:39], v[60:63], v[56:59], v[36:39]
	v_mfma_f32_16x16x32_f16 v[44:47], v[64:67], v[56:59], v[44:47]
	v_mfma_f32_16x16x32_f16 v[28:31], v[68:71], v[56:59], v[28:31]
	v_mfma_f32_16x16x32_f16 v[20:23], v[72:75], v[56:59], v[20:23]
	ds_read_b128 v[52:55], v10
	ds_read_b128 v[56:59], v10 offset:2048
	ds_read_b128 v[60:63], v9 offset:16384
	ds_read_b128 v[64:67], v9 offset:18432
	ds_read_b128 v[68:71], v9 offset:20480
	ds_read_b128 v[72:75], v9 offset:22528
	s_waitcnt lgkmcnt(0)
	v_mfma_f32_16x16x32_f16 v[24:27], v[84:87], v[76:79], v[24:27]
	v_mfma_f32_16x16x32_f16 v[32:35], v[88:91], v[76:79], v[32:35]
	v_mfma_f32_16x16x32_f16 v[40:43], v[92:95], v[76:79], v[40:43]
	v_mfma_f32_16x16x32_f16 v[48:51], v[96:99], v[76:79], v[48:51]
	v_mfma_f32_16x16x32_f16 v[36:39], v[84:87], v[80:83], v[36:39]
	v_mfma_f32_16x16x32_f16 v[44:47], v[88:91], v[80:83], v[44:47]
	v_mfma_f32_16x16x32_f16 v[28:31], v[92:95], v[80:83], v[28:31]
	v_mfma_f32_16x16x32_f16 v[20:23], v[96:99], v[80:83], v[20:23]
	s_mov_b64 s[20:21], 0x480
	s_mov_b32 m0, s6
	s_waitcnt vmcnt(4) lgkmcnt(0)
	s_barrier
	v_lshl_add_u64 v[76:77], v[4:5], 0, s[20:21]
	v_lshl_add_u64 v[78:79], v[6:7], 0, s[20:21]
	s_mov_b64 s[20:21], 0x20480
	global_load_lds_dwordx4 v[78:79], off
	v_lshl_add_u64 v[78:79], v[6:7], 0, s[20:21]
	s_mov_b32 m0, s3
	s_nop 0
	global_load_lds_dwordx4 v[78:79], off
	s_mov_b32 m0, s4
	s_nop 0
	global_load_lds_dwordx4 v[76:77], off
	v_lshl_add_u64 v[76:77], v[4:5], 0, s[20:21]
	s_mov_b32 m0, s5
	s_nop 0
	global_load_lds_dwordx4 v[76:77], off
	ds_read_b128 v[76:79], v11 offset:32768
	ds_read_b128 v[80:83], v11 offset:34816
	ds_read_b128 v[84:87], v2 offset:49152
	ds_read_b128 v[88:91], v2 offset:51200
	ds_read_b128 v[92:95], v2 offset:53248
	ds_read_b128 v[96:99], v2 offset:55296
	v_mfma_f32_16x16x32_f16 v[24:27], v[60:63], v[52:55], v[24:27]
	v_mfma_f32_16x16x32_f16 v[32:35], v[64:67], v[52:55], v[32:35]
	v_mfma_f32_16x16x32_f16 v[40:43], v[68:71], v[52:55], v[40:43]
	v_mfma_f32_16x16x32_f16 v[48:51], v[72:75], v[52:55], v[48:51]
	v_mfma_f32_16x16x32_f16 v[36:39], v[60:63], v[56:59], v[36:39]
	v_mfma_f32_16x16x32_f16 v[44:47], v[64:67], v[56:59], v[44:47]
	v_mfma_f32_16x16x32_f16 v[28:31], v[68:71], v[56:59], v[28:31]
	v_mfma_f32_16x16x32_f16 v[20:23], v[72:75], v[56:59], v[20:23]
	ds_read_b128 v[52:55], v10 offset:32768
	ds_read_b128 v[56:59], v10 offset:34816
	ds_read_b128 v[60:63], v9 offset:49152
	ds_read_b128 v[64:67], v9 offset:51200
	ds_read_b128 v[68:71], v9 offset:53248
	ds_read_b128 v[72:75], v9 offset:55296
	s_waitcnt lgkmcnt(0)
	v_mfma_f32_16x16x32_f16 v[24:27], v[84:87], v[76:79], v[24:27]
	v_mfma_f32_16x16x32_f16 v[32:35], v[88:91], v[76:79], v[32:35]
	v_mfma_f32_16x16x32_f16 v[40:43], v[92:95], v[76:79], v[40:43]
	v_mfma_f32_16x16x32_f16 v[48:51], v[96:99], v[76:79], v[48:51]
	v_mfma_f32_16x16x32_f16 v[36:39], v[84:87], v[80:83], v[36:39]
	v_mfma_f32_16x16x32_f16 v[44:47], v[88:91], v[80:83], v[44:47]
	v_mfma_f32_16x16x32_f16 v[28:31], v[92:95], v[80:83], v[28:31]
	v_mfma_f32_16x16x32_f16 v[20:23], v[96:99], v[80:83], v[20:23]
	s_mov_b64 s[20:21], 0x500
	s_mov_b32 m0, s16
	s_waitcnt vmcnt(4) lgkmcnt(0)
	s_barrier
	v_lshl_add_u64 v[76:77], v[4:5], 0, s[20:21]
	v_lshl_add_u64 v[78:79], v[6:7], 0, s[20:21]
	s_mov_b64 s[20:21], 0x20500
	global_load_lds_dwordx4 v[78:79], off
	v_lshl_add_u64 v[78:79], v[6:7], 0, s[20:21]
	s_mov_b32 m0, s13
	s_nop 0
	global_load_lds_dwordx4 v[78:79], off
	s_mov_b32 m0, s14
	s_nop 0
	global_load_lds_dwordx4 v[76:77], off
	v_lshl_add_u64 v[76:77], v[4:5], 0, s[20:21]
	s_mov_b32 m0, s15
	s_nop 0
	global_load_lds_dwordx4 v[76:77], off
	ds_read_b128 v[76:79], v12
	ds_read_b128 v[80:83], v13
	ds_read_b128 v[84:87], v14
	ds_read_b128 v[88:91], v15
	ds_read_b128 v[92:95], v16
	ds_read_b128 v[96:99], v17
	v_mfma_f32_16x16x32_f16 v[24:27], v[60:63], v[52:55], v[24:27]
	v_mfma_f32_16x16x32_f16 v[32:35], v[64:67], v[52:55], v[32:35]
	v_mfma_f32_16x16x32_f16 v[40:43], v[68:71], v[52:55], v[40:43]
	v_mfma_f32_16x16x32_f16 v[48:51], v[72:75], v[52:55], v[48:51]
	v_mfma_f32_16x16x32_f16 v[36:39], v[60:63], v[56:59], v[36:39]
	v_mfma_f32_16x16x32_f16 v[44:47], v[64:67], v[56:59], v[44:47]
	v_mfma_f32_16x16x32_f16 v[28:31], v[68:71], v[56:59], v[28:31]
	v_mfma_f32_16x16x32_f16 v[20:23], v[72:75], v[56:59], v[20:23]
	ds_read_b128 v[52:55], v19
	ds_read_b128 v[56:59], v19 offset:2048
	ds_read_b128 v[60:63], v18 offset:16384
	ds_read_b128 v[64:67], v18 offset:18432
	ds_read_b128 v[68:71], v18 offset:20480
	ds_read_b128 v[72:75], v18 offset:22528
	s_waitcnt lgkmcnt(0)
	v_mfma_f32_16x16x32_f16 v[24:27], v[84:87], v[76:79], v[24:27]
	v_mfma_f32_16x16x32_f16 v[32:35], v[88:91], v[76:79], v[32:35]
	v_mfma_f32_16x16x32_f16 v[40:43], v[92:95], v[76:79], v[40:43]
	v_mfma_f32_16x16x32_f16 v[48:51], v[96:99], v[76:79], v[48:51]
	v_mfma_f32_16x16x32_f16 v[36:39], v[84:87], v[80:83], v[36:39]
	v_mfma_f32_16x16x32_f16 v[44:47], v[88:91], v[80:83], v[44:47]
	v_mfma_f32_16x16x32_f16 v[28:31], v[92:95], v[80:83], v[28:31]
	v_mfma_f32_16x16x32_f16 v[20:23], v[96:99], v[80:83], v[20:23]
	s_mov_b64 s[20:21], 0x580
	s_mov_b32 m0, s18
	s_waitcnt vmcnt(4) lgkmcnt(0)
	s_barrier
	v_lshl_add_u64 v[76:77], v[4:5], 0, s[20:21]
	v_lshl_add_u64 v[78:79], v[6:7], 0, s[20:21]
	s_mov_b64 s[20:21], 0x20580
	global_load_lds_dwordx4 v[78:79], off
	v_lshl_add_u64 v[78:79], v[6:7], 0, s[20:21]
	s_mov_b32 m0, s17
	s_nop 0
	global_load_lds_dwordx4 v[78:79], off
	s_mov_b32 m0, s7
	s_nop 0
	global_load_lds_dwordx4 v[76:77], off
	v_lshl_add_u64 v[76:77], v[4:5], 0, s[20:21]
	s_mov_b32 m0, s12
	s_nop 0
	global_load_lds_dwordx4 v[76:77], off
	ds_read_b128 v[76:79], v11
	ds_read_b128 v[80:83], v11 offset:2048
	ds_read_b128 v[84:87], v2 offset:16384
	ds_read_b128 v[88:91], v2 offset:18432
	ds_read_b128 v[92:95], v2 offset:20480
	ds_read_b128 v[96:99], v2 offset:22528
	v_mfma_f32_16x16x32_f16 v[24:27], v[60:63], v[52:55], v[24:27]
	v_mfma_f32_16x16x32_f16 v[32:35], v[64:67], v[52:55], v[32:35]
	v_mfma_f32_16x16x32_f16 v[40:43], v[68:71], v[52:55], v[40:43]
	v_mfma_f32_16x16x32_f16 v[48:51], v[72:75], v[52:55], v[48:51]
	v_mfma_f32_16x16x32_f16 v[36:39], v[60:63], v[56:59], v[36:39]
	v_mfma_f32_16x16x32_f16 v[44:47], v[64:67], v[56:59], v[44:47]
	v_mfma_f32_16x16x32_f16 v[28:31], v[68:71], v[56:59], v[28:31]
	v_mfma_f32_16x16x32_f16 v[20:23], v[72:75], v[56:59], v[20:23]
	ds_read_b128 v[52:55], v10
	ds_read_b128 v[56:59], v10 offset:2048
	ds_read_b128 v[60:63], v9 offset:16384
	ds_read_b128 v[64:67], v9 offset:18432
	ds_read_b128 v[68:71], v9 offset:20480
	ds_read_b128 v[72:75], v9 offset:22528
	s_waitcnt lgkmcnt(0)
	v_mfma_f32_16x16x32_f16 v[24:27], v[84:87], v[76:79], v[24:27]
	v_mfma_f32_16x16x32_f16 v[32:35], v[88:91], v[76:79], v[32:35]
	v_mfma_f32_16x16x32_f16 v[40:43], v[92:95], v[76:79], v[40:43]
	v_mfma_f32_16x16x32_f16 v[48:51], v[96:99], v[76:79], v[48:51]
	v_mfma_f32_16x16x32_f16 v[36:39], v[84:87], v[80:83], v[36:39]
	v_mfma_f32_16x16x32_f16 v[44:47], v[88:91], v[80:83], v[44:47]
	v_mfma_f32_16x16x32_f16 v[28:31], v[92:95], v[80:83], v[28:31]
	v_mfma_f32_16x16x32_f16 v[20:23], v[96:99], v[80:83], v[20:23]
	s_mov_b64 s[20:21], 0x600
	s_mov_b32 m0, s6
	s_waitcnt vmcnt(4) lgkmcnt(0)
	s_barrier
	v_lshl_add_u64 v[76:77], v[4:5], 0, s[20:21]
	v_lshl_add_u64 v[78:79], v[6:7], 0, s[20:21]
	s_mov_b64 s[20:21], 0x20600
	global_load_lds_dwordx4 v[78:79], off
	v_lshl_add_u64 v[78:79], v[6:7], 0, s[20:21]
	s_mov_b32 m0, s3
	s_nop 0
	global_load_lds_dwordx4 v[78:79], off
	s_mov_b32 m0, s4
	s_nop 0
	global_load_lds_dwordx4 v[76:77], off
	v_lshl_add_u64 v[76:77], v[4:5], 0, s[20:21]
	s_mov_b32 m0, s5
	s_nop 0
	global_load_lds_dwordx4 v[76:77], off
	ds_read_b128 v[76:79], v11 offset:32768
	ds_read_b128 v[80:83], v11 offset:34816
	ds_read_b128 v[84:87], v2 offset:49152
	ds_read_b128 v[88:91], v2 offset:51200
	ds_read_b128 v[92:95], v2 offset:53248
	ds_read_b128 v[96:99], v2 offset:55296
	v_mfma_f32_16x16x32_f16 v[24:27], v[60:63], v[52:55], v[24:27]
	v_mfma_f32_16x16x32_f16 v[32:35], v[64:67], v[52:55], v[32:35]
	v_mfma_f32_16x16x32_f16 v[40:43], v[68:71], v[52:55], v[40:43]
	v_mfma_f32_16x16x32_f16 v[48:51], v[72:75], v[52:55], v[48:51]
	v_mfma_f32_16x16x32_f16 v[36:39], v[60:63], v[56:59], v[36:39]
	v_mfma_f32_16x16x32_f16 v[44:47], v[64:67], v[56:59], v[44:47]
	v_mfma_f32_16x16x32_f16 v[28:31], v[68:71], v[56:59], v[28:31]
	v_mfma_f32_16x16x32_f16 v[20:23], v[72:75], v[56:59], v[20:23]
	ds_read_b128 v[52:55], v10 offset:32768
	ds_read_b128 v[56:59], v10 offset:34816
	ds_read_b128 v[60:63], v9 offset:49152
	ds_read_b128 v[64:67], v9 offset:51200
	ds_read_b128 v[68:71], v9 offset:53248
	ds_read_b128 v[72:75], v9 offset:55296
	s_waitcnt lgkmcnt(0)
	v_mfma_f32_16x16x32_f16 v[24:27], v[84:87], v[76:79], v[24:27]
	v_mfma_f32_16x16x32_f16 v[32:35], v[88:91], v[76:79], v[32:35]
	v_mfma_f32_16x16x32_f16 v[40:43], v[92:95], v[76:79], v[40:43]
	v_mfma_f32_16x16x32_f16 v[48:51], v[96:99], v[76:79], v[48:51]
	v_mfma_f32_16x16x32_f16 v[36:39], v[84:87], v[80:83], v[36:39]
	v_mfma_f32_16x16x32_f16 v[44:47], v[88:91], v[80:83], v[44:47]
	v_mfma_f32_16x16x32_f16 v[28:31], v[92:95], v[80:83], v[28:31]
	v_mfma_f32_16x16x32_f16 v[20:23], v[96:99], v[80:83], v[20:23]
	s_mov_b64 s[20:21], 0x680
	s_mov_b32 m0, s16
	s_waitcnt vmcnt(4) lgkmcnt(0)
	s_barrier
	v_lshl_add_u64 v[76:77], v[4:5], 0, s[20:21]
	v_lshl_add_u64 v[78:79], v[6:7], 0, s[20:21]
	s_mov_b64 s[20:21], 0x20680
	global_load_lds_dwordx4 v[78:79], off
	v_lshl_add_u64 v[78:79], v[6:7], 0, s[20:21]
	s_mov_b32 m0, s13
	s_nop 0
	global_load_lds_dwordx4 v[78:79], off
	s_mov_b32 m0, s14
	s_nop 0
	global_load_lds_dwordx4 v[76:77], off
	v_lshl_add_u64 v[76:77], v[4:5], 0, s[20:21]
	s_mov_b32 m0, s15
	s_nop 0
	global_load_lds_dwordx4 v[76:77], off
	ds_read_b128 v[76:79], v12
	ds_read_b128 v[80:83], v13
	ds_read_b128 v[84:87], v14
	ds_read_b128 v[88:91], v15
	ds_read_b128 v[92:95], v16
	ds_read_b128 v[96:99], v17
	v_mfma_f32_16x16x32_f16 v[24:27], v[60:63], v[52:55], v[24:27]
	v_mfma_f32_16x16x32_f16 v[32:35], v[64:67], v[52:55], v[32:35]
	v_mfma_f32_16x16x32_f16 v[40:43], v[68:71], v[52:55], v[40:43]
	v_mfma_f32_16x16x32_f16 v[48:51], v[72:75], v[52:55], v[48:51]
	v_mfma_f32_16x16x32_f16 v[36:39], v[60:63], v[56:59], v[36:39]
	v_mfma_f32_16x16x32_f16 v[44:47], v[64:67], v[56:59], v[44:47]
	v_mfma_f32_16x16x32_f16 v[28:31], v[68:71], v[56:59], v[28:31]
	v_mfma_f32_16x16x32_f16 v[20:23], v[72:75], v[56:59], v[20:23]
	ds_read_b128 v[52:55], v19
	ds_read_b128 v[56:59], v19 offset:2048
	ds_read_b128 v[60:63], v18 offset:16384
	ds_read_b128 v[64:67], v18 offset:18432
	ds_read_b128 v[68:71], v18 offset:20480
	ds_read_b128 v[72:75], v18 offset:22528
	s_waitcnt lgkmcnt(0)
	v_mfma_f32_16x16x32_f16 v[24:27], v[84:87], v[76:79], v[24:27]
	v_mfma_f32_16x16x32_f16 v[32:35], v[88:91], v[76:79], v[32:35]
	v_mfma_f32_16x16x32_f16 v[40:43], v[92:95], v[76:79], v[40:43]
	v_mfma_f32_16x16x32_f16 v[48:51], v[96:99], v[76:79], v[48:51]
	v_mfma_f32_16x16x32_f16 v[36:39], v[84:87], v[80:83], v[36:39]
	v_mfma_f32_16x16x32_f16 v[44:47], v[88:91], v[80:83], v[44:47]
	v_mfma_f32_16x16x32_f16 v[28:31], v[92:95], v[80:83], v[28:31]
	v_mfma_f32_16x16x32_f16 v[20:23], v[96:99], v[80:83], v[20:23]
	s_mov_b64 s[14:15], 0x700
	s_mov_b32 m0, s18
	s_waitcnt vmcnt(4) lgkmcnt(0)
	s_barrier
	v_lshl_add_u64 v[76:77], v[4:5], 0, s[14:15]
	v_lshl_add_u64 v[78:79], v[6:7], 0, s[14:15]
	s_mov_b64 s[14:15], 0x20700
	global_load_lds_dwordx4 v[78:79], off
	v_lshl_add_u64 v[78:79], v[6:7], 0, s[14:15]
	s_mov_b32 m0, s17
	s_nop 0
	global_load_lds_dwordx4 v[78:79], off
	s_mov_b32 m0, s7
	s_nop 0
	global_load_lds_dwordx4 v[76:77], off
	v_lshl_add_u64 v[76:77], v[4:5], 0, s[14:15]
	s_mov_b32 m0, s12
	s_nop 0
	global_load_lds_dwordx4 v[76:77], off
	ds_read_b128 v[76:79], v11
	ds_read_b128 v[80:83], v11 offset:2048
	ds_read_b128 v[84:87], v2 offset:16384
	ds_read_b128 v[88:91], v2 offset:18432
	ds_read_b128 v[92:95], v2 offset:20480
	ds_read_b128 v[96:99], v2 offset:22528
	v_mfma_f32_16x16x32_f16 v[24:27], v[60:63], v[52:55], v[24:27]
	v_mfma_f32_16x16x32_f16 v[32:35], v[64:67], v[52:55], v[32:35]
	v_mfma_f32_16x16x32_f16 v[40:43], v[68:71], v[52:55], v[40:43]
	v_mfma_f32_16x16x32_f16 v[48:51], v[72:75], v[52:55], v[48:51]
	v_mfma_f32_16x16x32_f16 v[36:39], v[60:63], v[56:59], v[36:39]
	v_mfma_f32_16x16x32_f16 v[44:47], v[64:67], v[56:59], v[44:47]
	v_mfma_f32_16x16x32_f16 v[28:31], v[68:71], v[56:59], v[28:31]
	v_mfma_f32_16x16x32_f16 v[20:23], v[72:75], v[56:59], v[20:23]
	ds_read_b128 v[52:55], v10
	ds_read_b128 v[56:59], v10 offset:2048
	ds_read_b128 v[60:63], v9 offset:16384
	ds_read_b128 v[64:67], v9 offset:18432
	ds_read_b128 v[68:71], v9 offset:20480
	ds_read_b128 v[72:75], v9 offset:22528
	s_waitcnt lgkmcnt(0)
	v_mfma_f32_16x16x32_f16 v[24:27], v[84:87], v[76:79], v[24:27]
	v_mfma_f32_16x16x32_f16 v[32:35], v[88:91], v[76:79], v[32:35]
	v_mfma_f32_16x16x32_f16 v[40:43], v[92:95], v[76:79], v[40:43]
	v_mfma_f32_16x16x32_f16 v[48:51], v[96:99], v[76:79], v[48:51]
	v_mfma_f32_16x16x32_f16 v[36:39], v[84:87], v[80:83], v[36:39]
	v_mfma_f32_16x16x32_f16 v[44:47], v[88:91], v[80:83], v[44:47]
	v_mfma_f32_16x16x32_f16 v[28:31], v[92:95], v[80:83], v[28:31]
	v_mfma_f32_16x16x32_f16 v[20:23], v[96:99], v[80:83], v[20:23]
	s_mov_b32 m0, s6
	s_mov_b64 s[6:7], 0x780
	s_waitcnt vmcnt(4) lgkmcnt(0)
	s_barrier
	v_lshl_add_u64 v[76:77], v[4:5], 0, s[6:7]
	v_lshl_add_u64 v[78:79], v[6:7], 0, s[6:7]
	s_mov_b64 s[6:7], 0x20780
	global_load_lds_dwordx4 v[78:79], off
	v_lshl_add_u64 v[6:7], v[6:7], 0, s[6:7]
	s_mov_b32 m0, s3
	v_lshl_add_u64 v[4:5], v[4:5], 0, s[6:7]
	global_load_lds_dwordx4 v[6:7], off
	s_mov_b32 m0, s4
	s_nop 0
	global_load_lds_dwordx4 v[76:77], off
	s_mov_b32 m0, s5
	s_nop 0
	global_load_lds_dwordx4 v[4:5], off
	ds_read_b128 v[4:7], v11 offset:32768
	ds_read_b128 v[76:79], v11 offset:34816
	ds_read_b128 v[80:83], v2 offset:49152
	ds_read_b128 v[84:87], v2 offset:51200
	ds_read_b128 v[88:91], v2 offset:53248
	ds_read_b128 v[92:95], v2 offset:55296
	v_mfma_f32_16x16x32_f16 v[24:27], v[60:63], v[52:55], v[24:27]
	v_mfma_f32_16x16x32_f16 v[32:35], v[64:67], v[52:55], v[32:35]
	v_mfma_f32_16x16x32_f16 v[40:43], v[68:71], v[52:55], v[40:43]
	v_mfma_f32_16x16x32_f16 v[48:51], v[72:75], v[52:55], v[48:51]
	v_mfma_f32_16x16x32_f16 v[36:39], v[60:63], v[56:59], v[36:39]
	v_mfma_f32_16x16x32_f16 v[44:47], v[64:67], v[56:59], v[44:47]
	v_mfma_f32_16x16x32_f16 v[28:31], v[68:71], v[56:59], v[28:31]
	v_mfma_f32_16x16x32_f16 v[20:23], v[72:75], v[56:59], v[20:23]
	s_waitcnt lgkmcnt(0)
	v_mfma_f32_16x16x32_f16 v[24:27], v[80:83], v[4:7], v[24:27]
	v_mfma_f32_16x16x32_f16 v[32:35], v[84:87], v[4:7], v[32:35]
	v_mfma_f32_16x16x32_f16 v[40:43], v[88:91], v[4:7], v[40:43]
	v_mfma_f32_16x16x32_f16 v[4:7], v[92:95], v[4:7], v[48:51]
	s_nop 2
	ds_read_b128 v[48:51], v10 offset:32768
	ds_read_b128 v[52:55], v10 offset:34816
	ds_read_b128 v[56:59], v9 offset:49152
	ds_read_b128 v[60:63], v9 offset:51200
	ds_read_b128 v[64:67], v9 offset:53248
	ds_read_b128 v[68:71], v9 offset:55296
	v_mfma_f32_16x16x32_f16 v[36:39], v[80:83], v[76:79], v[36:39]
	v_mfma_f32_16x16x32_f16 v[44:47], v[84:87], v[76:79], v[44:47]
	v_mfma_f32_16x16x32_f16 v[28:31], v[88:91], v[76:79], v[28:31]
	v_mfma_f32_16x16x32_f16 v[20:23], v[92:95], v[76:79], v[20:23]
	s_waitcnt vmcnt(4) lgkmcnt(0)
	s_barrier
	ds_read_b128 v[72:75], v12
	ds_read_b128 v[76:79], v13
	ds_read_b128 v[80:83], v14
	ds_read_b128 v[12:15], v15
	ds_read_b128 v[84:87], v16
	ds_read_b128 v[88:91], v17
	v_mfma_f32_16x16x32_f16 v[24:27], v[56:59], v[48:51], v[24:27]
	v_mfma_f32_16x16x32_f16 v[32:35], v[60:63], v[48:51], v[32:35]
	v_mfma_f32_16x16x32_f16 v[40:43], v[64:67], v[48:51], v[40:43]
	v_mfma_f32_16x16x32_f16 v[4:7], v[68:71], v[48:51], v[4:7]
	v_mfma_f32_16x16x32_f16 v[36:39], v[56:59], v[52:55], v[36:39]
	v_mfma_f32_16x16x32_f16 v[44:47], v[60:63], v[52:55], v[44:47]
	v_mfma_f32_16x16x32_f16 v[28:31], v[64:67], v[52:55], v[28:31]
	v_mfma_f32_16x16x32_f16 v[20:23], v[68:71], v[52:55], v[20:23]
	s_waitcnt lgkmcnt(0)
	v_mfma_f32_16x16x32_f16 v[32:35], v[12:15], v[72:75], v[32:35]
	v_mfma_f32_16x16x32_f16 v[12:15], v[12:15], v[76:79], v[44:47]
	s_nop 2
	ds_read_b128 v[44:47], v19
	ds_read_b128 v[48:51], v19 offset:2048
	ds_read_b128 v[52:55], v18 offset:16384
	ds_read_b128 v[56:59], v18 offset:18432
	ds_read_b128 v[60:63], v18 offset:20480
	ds_read_b128 v[16:19], v18 offset:22528
	v_mfma_f32_16x16x32_f16 v[24:27], v[80:83], v[72:75], v[24:27]
	v_mfma_f32_16x16x32_f16 v[40:43], v[84:87], v[72:75], v[40:43]
	v_mfma_f32_16x16x32_f16 v[4:7], v[88:91], v[72:75], v[4:7]
	v_mfma_f32_16x16x32_f16 v[36:39], v[80:83], v[76:79], v[36:39]
	v_mfma_f32_16x16x32_f16 v[28:31], v[84:87], v[76:79], v[28:31]
	v_mfma_f32_16x16x32_f16 v[20:23], v[88:91], v[76:79], v[20:23]
	s_waitcnt vmcnt(0) lgkmcnt(0)
	s_barrier
	ds_read_b128 v[64:67], v11
	ds_read_b128 v[68:71], v11 offset:2048
	ds_read_b128 v[72:75], v2 offset:16384
	ds_read_b128 v[76:79], v2 offset:18432
	ds_read_b128 v[80:83], v2 offset:20480
	ds_read_b128 v[84:87], v2 offset:22528
	v_mfma_f32_16x16x32_f16 v[24:27], v[52:55], v[44:47], v[24:27]
	v_mfma_f32_16x16x32_f16 v[32:35], v[56:59], v[44:47], v[32:35]
	v_mfma_f32_16x16x32_f16 v[40:43], v[60:63], v[44:47], v[40:43]
	v_mfma_f32_16x16x32_f16 v[4:7], v[16:19], v[44:47], v[4:7]
	v_mfma_f32_16x16x32_f16 v[36:39], v[52:55], v[48:51], v[36:39]
	v_mfma_f32_16x16x32_f16 v[12:15], v[56:59], v[48:51], v[12:15]
	v_mfma_f32_16x16x32_f16 v[28:31], v[60:63], v[48:51], v[28:31]
	v_mfma_f32_16x16x32_f16 v[16:19], v[16:19], v[48:51], v[20:23]
	s_waitcnt lgkmcnt(3)
	v_mfma_f32_16x16x32_f16 v[20:23], v[72:75], v[64:67], v[24:27]
	s_waitcnt lgkmcnt(2)
	v_mfma_f32_16x16x32_f16 v[24:27], v[76:79], v[64:67], v[32:35]
	s_waitcnt lgkmcnt(1)
	v_mfma_f32_16x16x32_f16 v[32:35], v[80:83], v[64:67], v[40:43]
	s_nop 2
	ds_read_b128 v[40:43], v10
	ds_read_b128 v[44:47], v10 offset:2048
	ds_read_b128 v[48:51], v9 offset:16384
	ds_read_b128 v[52:55], v9 offset:18432
	ds_read_b128 v[56:59], v9 offset:20480
	ds_read_b128 v[60:63], v9 offset:22528
	s_waitcnt lgkmcnt(6)
	v_mfma_f32_16x16x32_f16 v[4:7], v[84:87], v[64:67], v[4:7]
	v_mfma_f32_16x16x32_f16 v[36:39], v[72:75], v[68:71], v[36:39]
	v_mfma_f32_16x16x32_f16 v[12:15], v[76:79], v[68:71], v[12:15]
	v_mfma_f32_16x16x32_f16 v[28:31], v[80:83], v[68:71], v[28:31]
	v_mfma_f32_16x16x32_f16 v[16:19], v[84:87], v[68:71], v[16:19]
	s_waitcnt vmcnt(0) lgkmcnt(0)
	s_barrier
	v_and_b32_e32 v2, 64, v0
	v_lshrrev_b32_e32 v9, 6, v0
	v_mfma_f32_16x16x32_f16 v[20:23], v[48:51], v[40:43], v[20:23]
	v_mfma_f32_16x16x32_f16 v[24:27], v[52:55], v[40:43], v[24:27]
	v_mfma_f32_16x16x32_f16 v[32:35], v[56:59], v[40:43], v[32:35]
	v_mfma_f32_16x16x32_f16 v[4:7], v[60:63], v[40:43], v[4:7]
	v_mfma_f32_16x16x32_f16 v[36:39], v[48:51], v[44:47], v[36:39]
	v_mfma_f32_16x16x32_f16 v[10:13], v[52:55], v[44:47], v[12:15]
	v_mfma_f32_16x16x32_f16 v[28:31], v[56:59], v[44:47], v[28:31]
	v_mfma_f32_16x16x32_f16 v[14:17], v[60:63], v[44:47], v[16:19]
	s_movk_i32 s3, 0x2200
	v_mad_u32_u24 v9, v9, s3, 0
	s_nop 0
	v_and_b32_e32 v18, 48, v0
	v_mul_u32_u24_e32 v19, 0x110, v8
	v_add3_u32 v18, v9, v18, v19
	s_barrier
	ds_write_b128 v18, v[20:23]
	ds_write_b128 v18, v[24:27] offset:64
	ds_write_b128 v18, v[32:35] offset:128
	ds_write_b128 v18, v[4:7] offset:192
	ds_write_b128 v18, v[36:39] offset:4352
	ds_write_b128 v18, v[10:13] offset:4416
	ds_write_b128 v18, v[28:31] offset:4480
	ds_write_b128 v18, v[14:17] offset:4544
	v_lshlrev_b32_e32 v4, 2, v8
	v_or3_b32 v2, v4, v2, s2
	v_lshlrev_b64 v[10:11], 2, v[2:3]
	s_waitcnt lgkmcnt(0)
	v_lshl_add_u64 v[2:3], s[10:11], 0, v[10:11]
	v_mov_b32_e32 v2, v106
	v_mov_b32_e32 v3, v107
	v_mov_b32_e32 v4, v108
	v_mov_b32_e32 v5, v109
	v_bfe_u32 v0, v0, 4, 2
	v_lshlrev_b32_e32 v6, 4, v8
	v_mul_u32_u24_e32 v7, 0x110, v0
	v_add3_u32 v13, v9, v6, v7
	ds_read_b128 v[6:9], v13
	v_or3_b32 v12, s1, v1, v0
	v_mad_i64_i32 v[0:1], s[2:3], v12, s0, 0
	v_lshl_add_u64 v[0:1], v[0:1], 2, s[8:9]
	v_lshl_add_u64 v[0:1], v[0:1], 0, v[10:11]
	v_or_b32_e32 v14, 4, v12
	v_or_b32_e32 v15, 8, v12
	v_or_b32_e32 v16, 12, v12
	v_or_b32_e32 v17, 16, v12
	v_or_b32_e32 v18, 20, v12
	v_or_b32_e32 v19, 24, v12
	v_or_b32_e32 v12, 28, v12
	s_waitcnt vmcnt(0) lgkmcnt(0)
	v_pk_add_f32 v[8:9], v[4:5], v[8:9]
	v_pk_add_f32 v[6:7], v[2:3], v[6:7]
	s_nop 0
	global_store_dwordx4 v[0:1], v[6:9], off sc1
	s_nop 1
	ds_read_b128 v[6:9], v13 offset:1088
	v_mad_i64_i32 v[0:1], s[2:3], v14, s0, 0
	v_lshl_add_u64 v[0:1], v[0:1], 2, s[8:9]
	v_lshl_add_u64 v[0:1], v[0:1], 0, v[10:11]
	s_waitcnt lgkmcnt(0)
	v_pk_add_f32 v[8:9], v[4:5], v[8:9]
	v_pk_add_f32 v[6:7], v[2:3], v[6:7]
	s_nop 0
	global_store_dwordx4 v[0:1], v[6:9], off sc1
	s_nop 1
	ds_read_b128 v[6:9], v13 offset:2176
	v_mad_i64_i32 v[0:1], s[2:3], v15, s0, 0
	v_lshl_add_u64 v[0:1], v[0:1], 2, s[8:9]
	v_lshl_add_u64 v[0:1], v[0:1], 0, v[10:11]
	s_waitcnt lgkmcnt(0)
	v_pk_add_f32 v[8:9], v[4:5], v[8:9]
	v_pk_add_f32 v[6:7], v[2:3], v[6:7]
	s_nop 0
	global_store_dwordx4 v[0:1], v[6:9], off sc1
	s_nop 1
	ds_read_b128 v[6:9], v13 offset:3264
	v_mad_i64_i32 v[0:1], s[2:3], v16, s0, 0
	v_lshl_add_u64 v[0:1], v[0:1], 2, s[8:9]
	v_lshl_add_u64 v[0:1], v[0:1], 0, v[10:11]
	s_waitcnt lgkmcnt(0)
	v_pk_add_f32 v[8:9], v[4:5], v[8:9]
	v_pk_add_f32 v[6:7], v[2:3], v[6:7]
	s_nop 0
	global_store_dwordx4 v[0:1], v[6:9], off sc1
	s_nop 1
	ds_read_b128 v[6:9], v13 offset:4352
	v_mad_i64_i32 v[0:1], s[2:3], v17, s0, 0
	v_lshl_add_u64 v[0:1], v[0:1], 2, s[8:9]
	v_lshl_add_u64 v[0:1], v[0:1], 0, v[10:11]
	s_waitcnt lgkmcnt(0)
	v_pk_add_f32 v[8:9], v[4:5], v[8:9]
	v_pk_add_f32 v[6:7], v[2:3], v[6:7]
	s_nop 0
	global_store_dwordx4 v[0:1], v[6:9], off sc1
	s_nop 1
	ds_read_b128 v[6:9], v13 offset:5440
	v_mad_i64_i32 v[0:1], s[2:3], v18, s0, 0
	v_lshl_add_u64 v[0:1], v[0:1], 2, s[8:9]
	v_lshl_add_u64 v[0:1], v[0:1], 0, v[10:11]
	s_waitcnt lgkmcnt(0)
	v_pk_add_f32 v[8:9], v[4:5], v[8:9]
	v_pk_add_f32 v[6:7], v[2:3], v[6:7]
	s_nop 0
	global_store_dwordx4 v[0:1], v[6:9], off sc1
	s_nop 1
	ds_read_b128 v[6:9], v13 offset:6528
	v_mad_i64_i32 v[0:1], s[2:3], v19, s0, 0
	v_lshl_add_u64 v[0:1], v[0:1], 2, s[8:9]
	v_lshl_add_u64 v[0:1], v[0:1], 0, v[10:11]
	s_waitcnt lgkmcnt(0)
	v_pk_add_f32 v[8:9], v[4:5], v[8:9]
	v_pk_add_f32 v[6:7], v[2:3], v[6:7]
	s_nop 0
	global_store_dwordx4 v[0:1], v[6:9], off sc1
	s_nop 1
	ds_read_b128 v[6:9], v13 offset:7616
	v_mad_i64_i32 v[0:1], s[0:1], v12, s0, 0
	v_lshl_add_u64 v[0:1], v[0:1], 2, s[8:9]
	v_lshl_add_u64 v[0:1], v[0:1], 0, v[10:11]
	s_waitcnt lgkmcnt(0)
	v_pk_add_f32 v[4:5], v[4:5], v[8:9]
	v_pk_add_f32 v[2:3], v[2:3], v[6:7]
	s_nop 0
	global_store_dwordx4 v[0:1], v[2:5], off sc1
	s_nop 1
	s_endpgm

	.amdhsa_kernel _Z8gemm16_kILi128ELi128ELi1ELi3EEvPKDF16_S1_PvPKfi
		.amdhsa_group_segment_fixed_size 0
		.amdhsa_private_segment_fixed_size 0
		.amdhsa_kernarg_size 36
		.amdhsa_user_sgpr_count 2
		.amdhsa_user_sgpr_dispatch_ptr 0
		.amdhsa_user_sgpr_queue_ptr 0
		.amdhsa_user_sgpr_kernarg_segment_ptr 1
		.amdhsa_user_sgpr_dispatch_id 0
		.amdhsa_user_sgpr_kernarg_preload_length 0
		.amdhsa_user_sgpr_kernarg_preload_offset 0
		.amdhsa_user_sgpr_private_segment_size 0
		.amdhsa_uses_dynamic_stack 0
		.amdhsa_enable_private_segment 0
		.amdhsa_system_sgpr_workgroup_id_x 1
		.amdhsa_system_sgpr_workgroup_id_y 0
		.amdhsa_system_sgpr_workgroup_id_z 0
		.amdhsa_system_sgpr_workgroup_info 0
		.amdhsa_system_vgpr_workitem_id 0
		.amdhsa_next_free_vgpr 110
		.amdhsa_next_free_sgpr 22
		.amdhsa_accum_offset 112
		.amdhsa_reserve_vcc 0
		.amdhsa_float_round_mode_32 0
		.amdhsa_float_round_mode_16_64 0
		.amdhsa_float_denorm_mode_32 3
		.amdhsa_float_denorm_mode_16_64 3
		.amdhsa_dx10_clamp 1
		.amdhsa_ieee_mode 1
		.amdhsa_fp16_overflow 0
		.amdhsa_tg_split 0
		.amdhsa_exception_fp_ieee_invalid_op 0
		.amdhsa_exception_fp_denorm_src 0
		.amdhsa_exception_fp_ieee_div_zero 0
		.amdhsa_exception_fp_ieee_overflow 0
		.amdhsa_exception_fp_ieee_underflow 0
		.amdhsa_exception_fp_ieee_inexact 0
		.amdhsa_exception_int_div_zero 0
	.end_amdhsa_kernel

amdhsa.kernels:
  - .agpr_count:     0
    .args:
      - .address_space:  global
        .offset:         0
        .size:           8
        .value_kind:     global_buffer
      - .address_space:  global
        .offset:         8
        .size:           8
        .value_kind:     global_buffer
      - .address_space:  global
        .offset:         16
        .size:           8
        .value_kind:     global_buffer
      - .address_space:  global
        .offset:         24
        .size:           8
        .value_kind:     global_buffer
      - .address_space:  global
        .offset:         32
        .size:           8
        .value_kind:     global_buffer
      - .address_space:  global
        .offset:         40
        .size:           8
        .value_kind:     global_buffer
      - .address_space:  global
        .offset:         48
        .size:           8
        .value_kind:     global_buffer
      - .address_space:  global
        .offset:         56
        .size:           8
        .value_kind:     global_buffer
    .group_segment_fixed_size: 0
    .kernarg_segment_align: 8
    .kernarg_segment_size: 64
    .language:       OpenCL C
    .language_version:
      - 2
      - 0
    .max_flat_workgroup_size: 256
    .name:           _Z10cvt_kernelPKfS0_S0_S0_S0_PDF16_S1_S1_
    .private_segment_fixed_size: 0
    .sgpr_count:     20
    .sgpr_spill_count: 0
    .symbol:         _Z10cvt_kernelPKfS0_S0_S0_S0_PDF16_S1_S1_.kd
    .uniform_work_group_size: 1
    .uses_dynamic_stack: false
    .vgpr_count:     70
    .vgpr_spill_count: 0
    .wavefront_size: 64
  - .agpr_count:     0
    .args:
      - .address_space:  global
        .offset:         0
        .size:           8
        .value_kind:     global_buffer
      - .address_space:  global
        .offset:         8
        .size:           8
        .value_kind:     global_buffer
      - .address_space:  global
        .offset:         16
        .size:           8
        .value_kind:     global_buffer
      - .address_space:  global
        .offset:         24
        .size:           8
        .value_kind:     global_buffer
    .group_segment_fixed_size: 0
    .kernarg_segment_align: 8
    .kernarg_segment_size: 32
    .language:       OpenCL C
    .language_version:
      - 2
      - 0
    .max_flat_workgroup_size: 512
    .name:           _Z10attn64_fwdPKDF16_S0_S0_PDF16_
    .private_segment_fixed_size: 0
    .sgpr_count:     57
    .sgpr_spill_count: 0
    .symbol:         _Z10attn64_fwdPKDF16_S0_S0_PDF16_.kd
    .uniform_work_group_size: 1
    .uses_dynamic_stack: false
    .vgpr_count:     219
    .vgpr_spill_count: 0
    .wavefront_size: 64
  - .agpr_count:     0
    .args:
      - .address_space:  global
        .offset:         0
        .size:           8
        .value_kind:     global_buffer
      - .address_space:  global
        .offset:         8
        .size:           8
        .value_kind:     global_buffer
      - .address_space:  global
        .offset:         16
        .size:           8
        .value_kind:     global_buffer
      - .actual_access:  read_only
        .address_space:  global
        .offset:         24
        .size:           8
        .value_kind:     global_buffer
      - .offset:         32
        .size:           4
        .value_kind:     by_value
    .group_segment_fixed_size: 0
    .kernarg_segment_align: 8
    .kernarg_segment_size: 36
    .language:       OpenCL C
    .language_version:
      - 2
      - 0
    .max_flat_workgroup_size: 512
    .name:           _Z8gemm16_kILi256ELi192ELi0ELi2EEvPKDF16_S1_PvPKfi
    .private_segment_fixed_size: 0
    .sgpr_count:     30
    .sgpr_spill_count: 0
    .symbol:         _Z8gemm16_kILi256ELi192ELi0ELi2EEvPKDF16_S1_PvPKfi.kd
    .uniform_work_group_size: 1
    .uses_dynamic_stack: false
    .vgpr_count:     208
    .vgpr_spill_count: 0
    .wavefront_size: 64
  - .agpr_count:     0
    .args:
      - .address_space:  global
        .offset:         0
        .size:           8
        .value_kind:     global_buffer
      - .address_space:  global
        .offset:         8
        .size:           8
        .value_kind:     global_buffer
      - .address_space:  global
        .offset:         16
        .size:           8
        .value_kind:     global_buffer
      - .actual_access:  read_only
        .address_space:  global
        .offset:         24
        .size:           8
        .value_kind:     global_buffer
      - .offset:         32
        .size:           4
        .value_kind:     by_value
    .group_segment_fixed_size: 0
    .kernarg_segment_align: 8
    .kernarg_segment_size: 36
    .language:       OpenCL C
    .language_version:
      - 2
      - 0
    .max_flat_workgroup_size: 512
    .name:           _Z8gemm16_kILi128ELi128ELi1ELi3EEvPKDF16_S1_PvPKfi
    .private_segment_fixed_size: 0
    .sgpr_count:     28
    .sgpr_spill_count: 0
    .symbol:         _Z8gemm16_kILi128ELi128ELi1ELi3EEvPKDF16_S1_PvPKfi.kd
    .uniform_work_group_size: 1
    .uses_dynamic_stack: false
    .vgpr_count:     110
    .vgpr_spill_count: 0
    .wavefront_size: 64
